# attention loop common path hand-written in place (no register copies); outproj bias loads hoisted to kernel start
# speedup vs baseline: 1.0601x; 1.0176x over previous
.Lattn_fast:
	ds_read_b128 v[110:113], v75 offset:8192
	ds_read_b128 v[114:117], v75 offset:10240
	ds_read_b128 v[118:121], v75 offset:12288
	ds_read_b128 v[122:125], v75 offset:14336
	v_exp_f32_e32 v34, v34
	v_exp_f32_e32 v1, v1
	v_exp_f32_e32 v36, v36
	v_exp_f32_e32 v35, v35
	v_exp_f32_e32 v38, v38
	v_exp_f32_e32 v37, v37
	v_exp_f32_e32 v40, v40
	v_exp_f32_e32 v39, v39
	v_add_f32_e32 v84, 0, v34
	v_cvt_pk_f16_f32 v50, v34, v1
	v_add_f32_e32 v84, v84, v1
	v_cvt_pk_f16_f32 v51, v36, v35
	v_add_f32_e32 v84, v84, v36
	v_cvt_pk_f16_f32 v52, v38, v37
	v_add_f32_e32 v84, v84, v35
	v_cvt_pk_f16_f32 v53, v40, v39
	ds_read_b128 v[58:61], v73 offset:8192
	ds_read_b128 v[62:65], v73 offset:10240
	v_exp_f32_e32 v42, v42
	v_exp_f32_e32 v41, v41
	v_exp_f32_e32 v44, v44
	v_exp_f32_e32 v43, v43
	v_add_f32_e32 v84, v84, v38
	v_add_f32_e32 v84, v84, v37
	s_waitcnt lgkmcnt(2)
	v_mfma_f32_16x16x32_f16 v[26:29], v[110:113], v[50:53], v[26:29]
	v_mfma_f32_16x16x32_f16 v[22:25], v[114:117], v[50:53], v[22:25]
	v_mfma_f32_16x16x32_f16 v[18:21], v[118:121], v[50:53], v[18:21]
	v_mfma_f32_16x16x32_f16 v[14:17], v[122:125], v[50:53], v[14:17]
	ds_read_b128 v[110:113], v73 offset:12288
	ds_read_b128 v[114:117], v73 offset:14336
	v_exp_f32_e32 v46, v46
	v_exp_f32_e32 v45, v45
	v_exp_f32_e32 v48, v48
	v_exp_f32_e32 v47, v47
	v_add_f32_e32 v84, v84, v40
	v_cvt_pk_f16_f32 v54, v42, v41
	v_add_f32_e32 v84, v84, v39
	v_cvt_pk_f16_f32 v55, v44, v43
	v_add_f32_e32 v84, v84, v42
	v_cvt_pk_f16_f32 v56, v46, v45
	v_add_f32_e32 v84, v84, v41
	v_cvt_pk_f16_f32 v57, v48, v47
	v_add_f32_e32 v84, v84, v44
	v_add_f32_e32 v84, v84, v43
	v_add_f32_e32 v84, v84, v46
	v_add_f32_e32 v84, v84, v45
	v_add_f32_e32 v84, v84, v48
	v_add_f32_e32 v84, v84, v47
	s_waitcnt lgkmcnt(0)
	v_mfma_f32_16x16x32_f16 v[26:29], v[58:61], v[54:57], v[26:29]
	v_mfma_f32_16x16x32_f16 v[22:25], v[62:65], v[54:57], v[22:25]
	v_mfma_f32_16x16x32_f16 v[18:21], v[110:113], v[54:57], v[18:21]
	v_mfma_f32_16x16x32_f16 v[14:17], v[114:117], v[54:57], v[14:17]
	v_add_f32_e32 v68, v68, v84
	s_branch .LBB2_29

_Z14outproj_kernelPKDF16_S0_PKfPf:
	s_load_dwordx8 s[4:11], s[0:1], 0x0
	s_lshl_b32 s0, s2, 1
	s_and_b32 s0, s0, 8
	s_bfe_u32 s1, s2, 0x30003
	s_or_b32 s3, s0, s1
	s_lshl_b32 s0, s2, 2
	s_and_b32 s0, s0, 12
	s_lshr_b32 s1, s2, 6
	v_lshrrev_b32_e32 v1, 4, v0
	s_add_i32 s0, s0, s1
	s_lshl_b32 s0, s0, 7
	v_xor_b32_e32 v10, v1, v0
	s_ashr_i32 s1, s0, 31
	v_lshlrev_b32_e32 v3, 3, v10
	s_lshl_b32 s2, s3, 17
	s_lshl_b64 s[12:13], s[0:1], 11
	v_lshlrev_b32_e32 v2, 7, v0
	v_and_b32_e32 v3, 56, v3
	s_mov_b32 s1, 0xfc00
	v_and_or_b32 v4, v2, s1, v3
	v_or_b32_e32 v2, 0x10000, v2
	s_mov_b32 s1, 0x1fc00
	s_waitcnt lgkmcnt(0)
	v_lshrrev_b32_e32 v120, 8, v0
	v_bfe_u32 v121, v0, 4, 2
	v_lshlrev_b32_e32 v120, 5, v120
	s_lshl_b32 s24, s3, 6
	v_lshl_or_b32 v120, v121, 2, v120
	v_add_u32_e32 v120, s24, v120
	v_lshlrev_b32_e32 v120, 2, v120
	global_load_dwordx4 v[124:127], v120, s[8:9]
	global_load_dwordx4 v[128:131], v120, s[8:9] offset:64
	s_add_u32 s4, s4, s2
	v_lshlrev_b32_e32 v11, 4, v0
	v_and_or_b32 v8, v2, s1, v3
	s_addc_u32 s5, s5, 0
	v_lshrrev_b32_e32 v2, 3, v0
	v_readfirstlane_b32 s1, v11
	v_or_b32_e32 v9, 0x2000, v11
	s_add_u32 s6, s6, s12
	v_and_b32_e32 v13, 32, v2
	v_lshlrev_b32_e32 v2, 1, v4
	v_mov_b32_e32 v3, 0
	s_mov_b32 m0, s1
	v_readfirstlane_b32 s2, v9
	v_or_b32_e32 v16, 0x4000, v11
	s_addc_u32 s7, s7, s13
	v_lshl_add_u64 v[4:5], s[4:5], 0, v[2:3]
	global_load_lds_dwordx4 v2, s[4:5]
	s_mov_b32 m0, s2
	v_readfirstlane_b32 s4, v16
	v_lshl_add_u64 v[6:7], s[6:7], 0, v[2:3]
	global_load_lds_dwordx4 v2, s[6:7]
	v_lshlrev_b32_e32 v2, 1, v8
	s_mov_b32 m0, s4
	v_lshl_add_u64 v[8:9], s[6:7], 0, v[2:3]
	global_load_lds_dwordx4 v2, s[6:7]
	v_or_b32_e32 v2, 0x6000, v11
	s_mov_b64 s[6:7], 0x80
	v_readfirstlane_b32 s18, v2
	v_or_b32_e32 v2, 0x8000, v11
	v_lshl_add_u64 v[16:17], v[4:5], 0, s[6:7]
	s_mov_b32 m0, s18
	v_readfirstlane_b32 s19, v2
	v_or_b32_e32 v2, 0xa000, v11
	global_load_lds_dwordx4 v[16:17], off
	v_lshl_add_u64 v[16:17], v[6:7], 0, s[6:7]
	s_mov_b32 m0, s19
	v_readfirstlane_b32 s20, v2
	v_or_b32_e32 v2, 0xc000, v11
	global_load_lds_dwordx4 v[16:17], off
	v_lshl_add_u64 v[16:17], v[8:9], 0, s[6:7]
	s_mov_b32 m0, s20
	s_mov_b64 s[6:7], 0x100
	v_readfirstlane_b32 s15, v2
	v_or_b32_e32 v2, 0xe000, v11
	global_load_lds_dwordx4 v[16:17], off
	v_lshl_add_u64 v[16:17], v[4:5], 0, s[6:7]
	s_mov_b32 m0, s15
	v_readfirstlane_b32 s16, v2
	v_or_b32_e32 v2, 0x10000, v11
	global_load_lds_dwordx4 v[16:17], off
	v_lshl_add_u64 v[16:17], v[6:7], 0, s[6:7]
	s_mov_b32 m0, s16
	v_readfirstlane_b32 s17, v2
	v_or_b32_e32 v2, 0x12000, v11
	global_load_lds_dwordx4 v[16:17], off
	v_lshl_add_u64 v[16:17], v[8:9], 0, s[6:7]
	s_mov_b32 m0, s17
	s_mov_b64 s[6:7], 0x180
	v_readfirstlane_b32 s12, v2
	v_or_b32_e32 v2, 0x14000, v11
	global_load_lds_dwordx4 v[16:17], off
	v_lshl_add_u64 v[16:17], v[4:5], 0, s[6:7]
	s_mov_b32 m0, s12
	v_readfirstlane_b32 s13, v2
	v_or_b32_e32 v2, 0x16000, v11
	global_load_lds_dwordx4 v[16:17], off
	v_lshl_add_u64 v[16:17], v[6:7], 0, s[6:7]
	s_mov_b32 m0, s13
	v_readfirstlane_b32 s14, v2
	v_or_b32_e32 v2, 0x18000, v11
	global_load_lds_dwordx4 v[16:17], off
	v_lshl_add_u64 v[16:17], v[8:9], 0, s[6:7]
	s_mov_b32 m0, s14
	s_mov_b64 s[22:23], 0x200
	v_readfirstlane_b32 s5, v2
	v_or_b32_e32 v2, 0x1a000, v11
	global_load_lds_dwordx4 v[16:17], off
	v_lshl_add_u64 v[16:17], v[4:5], 0, s[22:23]
	s_mov_b32 m0, s5
	v_readfirstlane_b32 s7, v2
	v_or_b32_e32 v2, 0x1c000, v11
	global_load_lds_dwordx4 v[16:17], off
	v_lshl_add_u64 v[16:17], v[6:7], 0, s[22:23]
	s_mov_b32 m0, s7
	v_readfirstlane_b32 s6, v2
	v_and_b32_e32 v12, 15, v0
	v_bfe_u32 v14, v0, 4, 2
	v_lshrrev_b32_e32 v15, 1, v0
	global_load_lds_dwordx4 v[16:17], off
	v_lshl_add_u64 v[16:17], v[8:9], 0, s[22:23]
	s_mov_b32 m0, s6
	s_movk_i32 s21, 0x60
	global_load_lds_dwordx4 v[16:17], off
	v_or_b32_e32 v16, v13, v12
	v_and_or_b32 v2, v15, s21, v12
	v_bitop3_b32 v15, v15, v14, 7 bitop3:0x6c
	v_lshlrev_b32_e32 v84, 7, v2
	v_lshlrev_b32_e32 v85, 7, v16
	v_lshlrev_b32_e32 v86, 4, v15
	s_waitcnt vmcnt(12)
	s_barrier
	v_or_b32_e32 v15, v85, v86
	v_or_b32_e32 v17, v84, v86
	v_bfe_u32 v18, v0, 1, 3
	ds_read_b128 v[20:23], v15
	ds_read_b128 v[24:27], v15 offset:2048
	ds_read_b128 v[28:31], v17 offset:8192
	ds_read_b128 v[32:35], v17 offset:10240
	v_bitop3_b32 v16, v14, v18, 4 bitop3:0x36
	v_lshlrev_b32_e32 v87, 4, v16
	v_or_b32_e32 v16, v85, v87
	v_or_b32_e32 v18, v84, v87
	ds_read_b128 v[36:39], v16
	ds_read_b128 v[40:43], v16 offset:2048
	s_waitcnt lgkmcnt(0)
	v_mfma_f32_16x16x32_f16 v[44:47], v[20:23], v[28:31], 0
	ds_read_b128 v[48:51], v18 offset:8192
	ds_read_b128 v[52:55], v18 offset:10240
	s_waitcnt vmcnt(9)
	s_mov_b64 s[22:23], 0x280
	v_mfma_f32_16x16x32_f16 v[20:23], v[20:23], v[32:35], 0
	s_waitcnt lgkmcnt(0)
	s_barrier
	v_lshl_add_u64 v[56:57], v[4:5], 0, s[22:23]
	s_mov_b32 m0, s1
	v_mfma_f32_16x16x32_f16 v[28:31], v[24:27], v[28:31], 0
	global_load_lds_dwordx4 v[56:57], off
	v_lshl_add_u64 v[56:57], v[6:7], 0, s[22:23]
	s_mov_b32 m0, s2
	v_mfma_f32_16x16x32_f16 v[24:27], v[24:27], v[32:35], 0
	global_load_lds_dwordx4 v[56:57], off
	s_mov_b32 m0, s4
	s_waitcnt lgkmcnt(0)
	v_mfma_f32_16x16x32_f16 v[32:35], v[36:39], v[48:51], v[44:47]
	v_or_b32_e32 v19, 0x12000, v85
	v_lshlrev_b32_e32 v12, 2, v12
	v_lshlrev_b32_e32 v2, 8, v2
	v_lshl_add_u64 v[44:45], v[8:9], 0, s[22:23]
	global_load_lds_dwordx4 v[44:45], off
	v_mfma_f32_16x16x32_f16 v[20:23], v[36:39], v[52:55], v[20:23]
	ds_read_b128 v[36:39], v15 offset:24576
	ds_read_b128 v[44:47], v15 offset:26624
	s_mov_b64 s[22:23], 0x300
	s_mov_b32 m0, s18
	v_mfma_f32_16x16x32_f16 v[28:31], v[40:43], v[48:51], v[28:31]
	ds_read_b128 v[48:51], v17 offset:32768
	ds_read_b128 v[56:59], v17 offset:34816
	ds_read_b128 v[60:63], v16 offset:24576
	ds_read_b128 v[64:67], v16 offset:26624
	v_mfma_f32_16x16x32_f16 v[24:27], v[40:43], v[52:55], v[24:27]
	ds_read_b128 v[40:43], v18 offset:32768
	ds_read_b128 v[52:55], v18 offset:34816
	s_waitcnt vmcnt(9)
	s_waitcnt lgkmcnt(0)
	s_waitcnt lgkmcnt(0)
	v_mfma_f32_16x16x32_f16 v[32:35], v[36:39], v[48:51], v[32:35]
	s_barrier
	v_mfma_f32_16x16x32_f16 v[20:23], v[36:39], v[56:59], v[20:23]
	v_lshl_add_u64 v[36:37], v[4:5], 0, s[22:23]
	global_load_lds_dwordx4 v[36:37], off
	v_lshl_add_u64 v[36:37], v[6:7], 0, s[22:23]
	s_mov_b32 m0, s19
	v_mfma_f32_16x16x32_f16 v[28:31], v[44:47], v[48:51], v[28:31]
	global_load_lds_dwordx4 v[36:37], off
	v_lshl_add_u64 v[36:37], v[8:9], 0, s[22:23]
	s_mov_b32 m0, s20
	v_mfma_f32_16x16x32_f16 v[24:27], v[44:47], v[56:59], v[24:27]
	global_load_lds_dwordx4 v[36:37], off
	ds_read_b128 v[36:39], v15 offset:49152
	ds_read_b128 v[44:47], v15 offset:51200
	ds_read_b128 v[48:51], v17 offset:57344
	ds_read_b128 v[56:59], v17 offset:59392
	v_mfma_f32_16x16x32_f16 v[32:35], v[60:63], v[40:43], v[32:35]
	s_mov_b64 s[22:23], 0x380
	s_mov_b32 m0, s15
	v_mfma_f32_16x16x32_f16 v[20:23], v[60:63], v[52:55], v[20:23]
	v_mfma_f32_16x16x32_f16 v[28:31], v[64:67], v[40:43], v[28:31]
	ds_read_b128 v[40:43], v16 offset:49152
	ds_read_b128 v[60:63], v16 offset:51200
	ds_read_b128 v[68:71], v18 offset:57344
	ds_read_b128 v[72:75], v18 offset:59392
	s_waitcnt vmcnt(9)
	s_waitcnt lgkmcnt(0)
	v_mfma_f32_16x16x32_f16 v[52:55], v[64:67], v[52:55], v[24:27]
	s_barrier
	s_waitcnt lgkmcnt(0)
	v_mfma_f32_16x16x32_f16 v[32:35], v[36:39], v[48:51], v[32:35]
	v_lshl_add_u64 v[24:25], v[4:5], 0, s[22:23]
	global_load_lds_dwordx4 v[24:25], off
	v_lshl_add_u64 v[24:25], v[6:7], 0, s[22:23]
	s_mov_b32 m0, s16
	v_mfma_f32_16x16x32_f16 v[36:39], v[36:39], v[56:59], v[20:23]
	global_load_lds_dwordx4 v[24:25], off
	v_lshl_add_u64 v[24:25], v[8:9], 0, s[22:23]
	s_mov_b32 m0, s17
	v_or_b32_e32 v23, v19, v86
	global_load_lds_dwordx4 v[24:25], off
	v_or_b32_e32 v25, 0x14000, v84
	v_or_b32_e32 v21, 0x12800, v85
	v_mfma_f32_16x16x32_f16 v[26:29], v[44:47], v[48:51], v[28:31]
	v_or_b32_e32 v88, v25, v86
	v_or_b32_e32 v22, 0x14800, v84
	v_or_b32_e32 v24, v21, v86
	v_mfma_f32_16x16x32_f16 v[44:47], v[44:47], v[56:59], v[52:55]
	ds_read_b128 v[48:51], v23
	ds_read_b128 v[64:67], v24
	v_or_b32_e32 v89, v22, v86
	ds_read_b128 v[52:55], v88
	ds_read_b128 v[56:59], v89
	v_mfma_f32_16x16x32_f16 v[30:33], v[40:43], v[68:71], v[32:35]
	v_or_b32_e32 v20, v19, v87
	v_or_b32_e32 v19, v21, v87
	v_or_b32_e32 v21, v25, v87
	v_mfma_f32_16x16x32_f16 v[34:37], v[40:43], v[72:75], v[36:39]
	s_nop 2
	ds_read_b128 v[38:41], v20
	ds_read_b128 v[76:79], v19
	v_or_b32_e32 v22, v22, v87
	s_mov_b64 s[22:23], 0x400
	v_mfma_f32_16x16x32_f16 v[26:29], v[60:63], v[68:71], v[26:29]
	ds_read_b128 v[68:71], v21
	ds_read_b128 v[80:83], v22
	s_waitcnt vmcnt(9)
	s_waitcnt lgkmcnt(0)
	v_mfma_f32_16x16x32_f16 v[42:45], v[60:63], v[72:75], v[44:47]
	s_barrier
	s_mov_b32 m0, s12
	s_waitcnt lgkmcnt(0)
	v_mfma_f32_16x16x32_f16 v[30:33], v[48:51], v[52:55], v[30:33]
	v_lshl_add_u64 v[46:47], v[4:5], 0, s[22:23]
	global_load_lds_dwordx4 v[46:47], off
	v_mfma_f32_16x16x32_f16 v[34:37], v[48:51], v[56:59], v[34:37]
	v_lshl_add_u64 v[46:47], v[6:7], 0, s[22:23]
	s_mov_b32 m0, s13
	v_add_u32_e32 v25, 0x1a000, v84
	v_mfma_f32_16x16x32_f16 v[26:29], v[64:67], v[52:55], v[26:29]
	global_load_lds_dwordx4 v[46:47], off
	v_lshl_add_u64 v[46:47], v[8:9], 0, s[22:23]
	v_mfma_f32_16x16x32_f16 v[42:45], v[64:67], v[56:59], v[42:45]
	s_mov_b32 m0, s14
	v_or_b32_e32 v58, 0x18000, v85
	v_add_u32_e32 v66, 0x1a800, v84
	global_load_lds_dwordx4 v[46:47], off
	v_or_b32_e32 v74, v58, v86
	v_or_b32_e32 v59, 0x18800, v85
	v_or_b32_e32 v85, v25, v86
	v_or_b32_e32 v84, v66, v86
	v_mfma_f32_16x16x32_f16 v[30:33], v[38:41], v[68:71], v[30:33]
	v_or_b32_e32 v75, v59, v86
	s_mov_b64 s[22:23], 0x480
	s_mov_b32 m0, s5
	v_mfma_f32_16x16x32_f16 v[34:37], v[38:41], v[80:83], v[34:37]
	ds_read_b128 v[38:41], v74
	ds_read_b128 v[46:49], v75
	ds_read_b128 v[50:53], v85
	ds_read_b128 v[54:57], v84
	v_mfma_f32_16x16x32_f16 v[26:29], v[76:79], v[68:71], v[26:29]
	v_mfma_f32_16x16x32_f16 v[42:45], v[76:79], v[80:83], v[42:45]
	v_or_b32_e32 v76, v58, v87
	v_or_b32_e32 v78, v25, v87
	v_or_b32_e32 v77, v59, v87
	s_waitcnt lgkmcnt(0)
	v_mfma_f32_16x16x32_f16 v[30:33], v[38:41], v[50:53], v[30:33]
	ds_read_b128 v[58:61], v76
	ds_read_b128 v[62:65], v77
	v_or_b32_e32 v79, v66, v87
	v_mfma_f32_16x16x32_f16 v[34:37], v[38:41], v[54:57], v[34:37]
	ds_read_b128 v[38:41], v78
	ds_read_b128 v[66:69], v79
	s_waitcnt vmcnt(9)
	s_waitcnt lgkmcnt(0)
	v_mfma_f32_16x16x32_f16 v[26:29], v[46:49], v[50:53], v[26:29]
	s_barrier
	v_lshl_add_u64 v[50:51], v[8:9], 0, s[22:23]
	v_mfma_f32_16x16x32_f16 v[42:45], v[46:49], v[54:57], v[42:45]
	v_lshl_add_u64 v[46:47], v[4:5], 0, s[22:23]
	global_load_lds_dwordx4 v[46:47], off
	v_lshl_add_u64 v[46:47], v[6:7], 0, s[22:23]
	s_mov_b32 m0, s7
	s_waitcnt lgkmcnt(0)
	v_mfma_f32_16x16x32_f16 v[30:33], v[58:61], v[38:41], v[30:33]
	global_load_lds_dwordx4 v[46:47], off
	ds_read_b128 v[46:49], v15
	s_mov_b32 m0, s6
	v_mfma_f32_16x16x32_f16 v[26:29], v[62:65], v[38:41], v[26:29]
	global_load_lds_dwordx4 v[50:51], off
	ds_read_b128 v[38:41], v15 offset:2048
	ds_read_b128 v[50:53], v17 offset:8192
	v_mfma_f32_16x16x32_f16 v[34:37], v[58:61], v[66:69], v[34:37]
	s_mov_b64 s[22:23], 0x500
	s_mov_b32 m0, s1
	v_mfma_f32_16x16x32_f16 v[42:45], v[62:65], v[66:69], v[42:45]
	ds_read_b128 v[54:57], v17 offset:10240
	ds_read_b128 v[58:61], v16
	ds_read_b128 v[62:65], v16 offset:2048
	ds_read_b128 v[66:69], v18 offset:8192
	ds_read_b128 v[70:73], v18 offset:10240
	s_waitcnt vmcnt(9)
	s_waitcnt lgkmcnt(0)
	v_mfma_f32_16x16x32_f16 v[30:33], v[46:49], v[50:53], v[30:33]
	s_waitcnt lgkmcnt(0)
	s_barrier
	v_mfma_f32_16x16x32_f16 v[34:37], v[46:49], v[54:57], v[34:37]
	v_lshl_add_u64 v[46:47], v[4:5], 0, s[22:23]
	global_load_lds_dwordx4 v[46:47], off
	v_mfma_f32_16x16x32_f16 v[26:29], v[38:41], v[50:53], v[26:29]
	s_mov_b32 m0, s2
	v_mfma_f32_16x16x32_f16 v[38:41], v[38:41], v[54:57], v[42:45]
	s_nop 2
	v_lshl_add_u64 v[42:43], v[6:7], 0, s[22:23]
	global_load_lds_dwordx4 v[42:43], off
	v_lshl_add_u64 v[42:43], v[8:9], 0, s[22:23]
	s_mov_b32 m0, s4
	v_mfma_f32_16x16x32_f16 v[30:33], v[58:61], v[66:69], v[30:33]
	global_load_lds_dwordx4 v[42:43], off
	ds_read_b128 v[42:45], v15 offset:24576
	ds_read_b128 v[46:49], v15 offset:26624
	ds_read_b128 v[50:53], v17 offset:32768
	v_mfma_f32_16x16x32_f16 v[34:37], v[58:61], v[70:73], v[34:37]
	s_mov_b64 s[22:23], 0x580
	s_mov_b32 m0, s18
	v_mfma_f32_16x16x32_f16 v[26:29], v[62:65], v[66:69], v[26:29]
	v_mfma_f32_16x16x32_f16 v[38:41], v[62:65], v[70:73], v[38:41]
	ds_read_b128 v[54:57], v17 offset:34816
	ds_read_b128 v[58:61], v16 offset:24576
	ds_read_b128 v[62:65], v16 offset:26624
	ds_read_b128 v[66:69], v18 offset:32768
	ds_read_b128 v[70:73], v18 offset:34816
	s_waitcnt vmcnt(9)
	s_waitcnt lgkmcnt(0)
	v_mfma_f32_16x16x32_f16 v[30:33], v[42:45], v[50:53], v[30:33]
	s_waitcnt lgkmcnt(0)
	s_barrier
	v_mfma_f32_16x16x32_f16 v[34:37], v[42:45], v[54:57], v[34:37]
	v_lshl_add_u64 v[42:43], v[4:5], 0, s[22:23]
	global_load_lds_dwordx4 v[42:43], off
	v_lshl_add_u64 v[42:43], v[6:7], 0, s[22:23]
	s_mov_b32 m0, s19
	v_mfma_f32_16x16x32_f16 v[26:29], v[46:49], v[50:53], v[26:29]
	global_load_lds_dwordx4 v[42:43], off
	v_lshl_add_u64 v[42:43], v[8:9], 0, s[22:23]
	v_mfma_f32_16x16x32_f16 v[38:41], v[46:49], v[54:57], v[38:41]
	s_mov_b32 m0, s20
	s_mov_b64 s[18:19], 0x600
	global_load_lds_dwordx4 v[42:43], off
	ds_read_b128 v[42:45], v15 offset:49152
	ds_read_b128 v[46:49], v15 offset:51200
	ds_read_b128 v[50:53], v17 offset:57344
	v_mfma_f32_16x16x32_f16 v[30:33], v[58:61], v[66:69], v[30:33]
	s_mov_b32 m0, s15
	v_mfma_f32_16x16x32_f16 v[34:37], v[58:61], v[70:73], v[34:37]
	v_mfma_f32_16x16x32_f16 v[26:29], v[62:65], v[66:69], v[26:29]
	v_mfma_f32_16x16x32_f16 v[38:41], v[62:65], v[70:73], v[38:41]
	ds_read_b128 v[54:57], v17 offset:59392
	ds_read_b128 v[58:61], v16 offset:49152
	ds_read_b128 v[62:65], v16 offset:51200
	ds_read_b128 v[66:69], v18 offset:57344
	ds_read_b128 v[70:73], v18 offset:59392
	s_waitcnt vmcnt(9)
	s_waitcnt lgkmcnt(0)
	v_mfma_f32_16x16x32_f16 v[30:33], v[42:45], v[50:53], v[30:33]
	s_waitcnt lgkmcnt(0)
	s_barrier
	v_mfma_f32_16x16x32_f16 v[34:37], v[42:45], v[54:57], v[34:37]
	v_lshl_add_u64 v[42:43], v[4:5], 0, s[18:19]
	global_load_lds_dwordx4 v[42:43], off
	v_lshl_add_u64 v[42:43], v[6:7], 0, s[18:19]
	s_mov_b32 m0, s16
	v_mfma_f32_16x16x32_f16 v[26:29], v[46:49], v[50:53], v[26:29]
	global_load_lds_dwordx4 v[42:43], off
	v_lshl_add_u64 v[42:43], v[8:9], 0, s[18:19]
	v_mfma_f32_16x16x32_f16 v[38:41], v[46:49], v[54:57], v[38:41]
	s_mov_b32 m0, s17
	s_mov_b64 s[16:17], 0x680
	global_load_lds_dwordx4 v[42:43], off
	ds_read_b128 v[42:45], v23
	ds_read_b128 v[46:49], v24
	ds_read_b128 v[50:53], v88
	v_mfma_f32_16x16x32_f16 v[30:33], v[58:61], v[66:69], v[30:33]
	s_mov_b32 m0, s12
	v_mfma_f32_16x16x32_f16 v[34:37], v[58:61], v[70:73], v[34:37]
	v_mfma_f32_16x16x32_f16 v[26:29], v[62:65], v[66:69], v[26:29]
	v_mfma_f32_16x16x32_f16 v[38:41], v[62:65], v[70:73], v[38:41]
	ds_read_b128 v[54:57], v89
	ds_read_b128 v[58:61], v20
	ds_read_b128 v[62:65], v19
	ds_read_b128 v[66:69], v21
	ds_read_b128 v[70:73], v22
	s_waitcnt vmcnt(9)
	s_waitcnt lgkmcnt(0)
	v_mfma_f32_16x16x32_f16 v[30:33], v[42:45], v[50:53], v[30:33]
	s_waitcnt lgkmcnt(0)
	s_barrier
	v_mfma_f32_16x16x32_f16 v[34:37], v[42:45], v[54:57], v[34:37]
	v_lshl_add_u64 v[42:43], v[4:5], 0, s[16:17]
	global_load_lds_dwordx4 v[42:43], off
	v_lshl_add_u64 v[42:43], v[6:7], 0, s[16:17]
	s_mov_b32 m0, s13
	v_mfma_f32_16x16x32_f16 v[26:29], v[46:49], v[50:53], v[26:29]
	global_load_lds_dwordx4 v[42:43], off
	v_lshl_add_u64 v[42:43], v[8:9], 0, s[16:17]
	s_mov_b32 m0, s14
	v_mfma_f32_16x16x32_f16 v[38:41], v[46:49], v[54:57], v[38:41]
	global_load_lds_dwordx4 v[42:43], off
	ds_read_b128 v[42:45], v74
	ds_read_b128 v[46:49], v85
	ds_read_b128 v[50:53], v75
	ds_read_b128 v[54:57], v84
	v_mfma_f32_16x16x32_f16 v[30:33], v[58:61], v[66:69], v[30:33]
	s_mov_b64 s[12:13], 0x700
	s_mov_b32 m0, s5
	v_mfma_f32_16x16x32_f16 v[34:37], v[58:61], v[70:73], v[34:37]
	v_mfma_f32_16x16x32_f16 v[26:29], v[62:65], v[66:69], v[26:29]
	v_mfma_f32_16x16x32_f16 v[38:41], v[62:65], v[70:73], v[38:41]
	ds_read_b128 v[58:61], v76
	ds_read_b128 v[62:65], v77
	s_waitcnt lgkmcnt(0)
	v_mfma_f32_16x16x32_f16 v[30:33], v[42:45], v[46:49], v[30:33]
	v_mfma_f32_16x16x32_f16 v[34:37], v[42:45], v[54:57], v[34:37]
	ds_read_b128 v[42:45], v78
	ds_read_b128 v[66:69], v79
	s_waitcnt vmcnt(9)
	s_waitcnt lgkmcnt(0)
	v_mfma_f32_16x16x32_f16 v[26:29], v[50:53], v[46:49], v[26:29]
	s_barrier
	v_lshl_add_u64 v[46:47], v[4:5], 0, s[12:13]
	global_load_lds_dwordx4 v[46:47], off
	v_lshl_add_u64 v[46:47], v[6:7], 0, s[12:13]
	s_mov_b32 m0, s7
	v_mfma_f32_16x16x32_f16 v[38:41], v[50:53], v[54:57], v[38:41]
	global_load_lds_dwordx4 v[46:47], off
	ds_read_b128 v[46:49], v15
	v_lshl_add_u64 v[50:51], v[8:9], 0, s[12:13]
	s_mov_b32 m0, s6
	s_waitcnt lgkmcnt(0)
	v_mfma_f32_16x16x32_f16 v[30:33], v[58:61], v[42:45], v[30:33]
	global_load_lds_dwordx4 v[50:51], off
	s_mov_b64 s[6:7], 0x780
	v_mfma_f32_16x16x32_f16 v[26:29], v[62:65], v[42:45], v[26:29]
	ds_read_b128 v[42:45], v15 offset:2048
	ds_read_b128 v[50:53], v17 offset:8192
	v_lshl_add_u64 v[4:5], v[4:5], 0, s[6:7]
	s_mov_b32 m0, s1
	v_mfma_f32_16x16x32_f16 v[34:37], v[58:61], v[66:69], v[34:37]
	v_lshl_add_u64 v[8:9], v[8:9], 0, s[6:7]
	s_lshl_b32 s1, s3, 8
	v_mfma_f32_16x16x32_f16 v[38:41], v[62:65], v[66:69], v[38:41]
	ds_read_b128 v[54:57], v17 offset:10240
	ds_read_b128 v[58:61], v16
	ds_read_b128 v[62:65], v16 offset:2048
	ds_read_b128 v[66:69], v18 offset:8192
	ds_read_b128 v[70:73], v18 offset:10240
	s_waitcnt vmcnt(9)
	s_waitcnt lgkmcnt(0)
	v_mfma_f32_16x16x32_f16 v[30:33], v[46:49], v[50:53], v[30:33]
	s_waitcnt lgkmcnt(0)
	s_barrier
	v_mfma_f32_16x16x32_f16 v[34:37], v[46:49], v[54:57], v[34:37]
	global_load_lds_dwordx4 v[4:5], off
	s_mov_b32 m0, s2
	v_mfma_f32_16x16x32_f16 v[26:29], v[42:45], v[50:53], v[26:29]
	s_add_u32 s2, s8, s1
	s_addc_u32 s3, s9, 0
	v_mfma_f32_16x16x32_f16 v[38:41], v[42:45], v[54:57], v[38:41]
	v_lshl_add_u64 v[42:43], v[6:7], 0, s[6:7]
	global_load_lds_dwordx4 v[42:43], off
	s_mov_b32 m0, s4
	v_mfma_f32_16x16x32_f16 v[4:7], v[58:61], v[66:69], v[30:33]
	global_load_lds_dwordx4 v[8:9], off
	v_lshlrev_b32_e32 v8, 2, v14
	v_mfma_f32_16x16x32_f16 v[30:33], v[58:61], v[70:73], v[34:37]
	v_or_b32_e32 v9, v8, v13
	v_lshlrev_b32_e32 v14, 2, v9
	v_bitop3_b32 v8, v8, v12, v13 bitop3:0x36
	ds_read_b128 v[34:37], v15 offset:24576
	ds_read_b128 v[42:45], v17 offset:32768
	ds_read_b128 v[46:49], v15 offset:26624
	ds_read_b128 v[50:53], v17 offset:34816
	v_mfma_f32_16x16x32_f16 v[26:29], v[62:65], v[66:69], v[26:29]
	v_lshl_or_b32 v8, v8, 2, v2
	v_mfma_f32_16x16x32_f16 v[38:41], v[62:65], v[70:73], v[38:41]
	s_waitcnt lgkmcnt(0)
	v_mfma_f32_16x16x32_f16 v[4:7], v[34:37], v[42:45], v[4:7]
	v_mfma_f32_16x16x32_f16 v[30:33], v[34:37], v[50:53], v[30:33]
	ds_read_b128 v[34:37], v16 offset:24576
	v_mfma_f32_16x16x32_f16 v[26:29], v[46:49], v[42:45], v[26:29]
	v_mfma_f32_16x16x32_f16 v[38:41], v[46:49], v[50:53], v[38:41]
	ds_read_b128 v[42:45], v18 offset:32768
	ds_read_b128 v[46:49], v16 offset:26624
	ds_read_b128 v[50:53], v18 offset:34816
	s_waitcnt vmcnt(9)
	s_waitcnt lgkmcnt(0)
	s_barrier
	s_waitcnt lgkmcnt(0)
	v_mfma_f32_16x16x32_f16 v[4:7], v[34:37], v[42:45], v[4:7]
	v_mfma_f32_16x16x32_f16 v[30:33], v[34:37], v[50:53], v[30:33]
	ds_read_b128 v[34:37], v15 offset:49152
	v_mfma_f32_16x16x32_f16 v[26:29], v[46:49], v[42:45], v[26:29]
	v_mfma_f32_16x16x32_f16 v[38:41], v[46:49], v[50:53], v[38:41]
	ds_read_b128 v[42:45], v17 offset:57344
	ds_read_b128 v[46:49], v15 offset:51200
	ds_read_b128 v[50:53], v17 offset:59392
	s_waitcnt lgkmcnt(0)
	v_mfma_f32_16x16x32_f16 v[4:7], v[34:37], v[42:45], v[4:7]
	v_mfma_f32_16x16x32_f16 v[30:33], v[34:37], v[50:53], v[30:33]
	ds_read_b128 v[34:37], v16 offset:49152
	v_mfma_f32_16x16x32_f16 v[26:29], v[46:49], v[42:45], v[26:29]
	v_mfma_f32_16x16x32_f16 v[38:41], v[46:49], v[50:53], v[38:41]
	ds_read_b128 v[42:45], v18 offset:57344
	ds_read_b128 v[46:49], v16 offset:51200
	ds_read_b128 v[50:53], v18 offset:59392
	s_waitcnt vmcnt(6)
	s_waitcnt lgkmcnt(0)
	s_barrier
	s_waitcnt lgkmcnt(0)
	v_mfma_f32_16x16x32_f16 v[4:7], v[34:37], v[42:45], v[4:7]
	v_mfma_f32_16x16x32_f16 v[30:33], v[34:37], v[50:53], v[30:33]
	ds_read_b128 v[34:37], v23
	v_mfma_f32_16x16x32_f16 v[26:29], v[46:49], v[42:45], v[26:29]
	v_mfma_f32_16x16x32_f16 v[38:41], v[46:49], v[50:53], v[38:41]
	ds_read_b128 v[42:45], v88
	ds_read_b128 v[46:49], v24
	ds_read_b128 v[50:53], v89
	s_waitcnt lgkmcnt(0)
	v_mfma_f32_16x16x32_f16 v[4:7], v[34:37], v[42:45], v[4:7]
	v_mfma_f32_16x16x32_f16 v[30:33], v[34:37], v[50:53], v[30:33]
	ds_read_b128 v[34:37], v20
	v_mfma_f32_16x16x32_f16 v[24:27], v[46:49], v[42:45], v[26:29]
	v_mfma_f32_16x16x32_f16 v[38:41], v[46:49], v[50:53], v[38:41]
	ds_read_b128 v[42:45], v21
	ds_read_b128 v[46:49], v19
	ds_read_b128 v[20:23], v22
	s_waitcnt vmcnt(3)
	s_waitcnt lgkmcnt(0)
	s_barrier
	s_waitcnt lgkmcnt(0)
	v_mfma_f32_16x16x32_f16 v[4:7], v[34:37], v[42:45], v[4:7]
	v_mfma_f32_16x16x32_f16 v[28:31], v[34:37], v[20:23], v[30:33]
	s_nop 2
	ds_read_b128 v[32:35], v74
	v_mfma_f32_16x16x32_f16 v[24:27], v[46:49], v[42:45], v[24:27]
	v_mfma_f32_16x16x32_f16 v[20:23], v[46:49], v[20:23], v[38:41]
	s_nop 2
	ds_read_b128 v[36:39], v85
	ds_read_b128 v[40:43], v75
	ds_read_b128 v[44:47], v84
	s_waitcnt lgkmcnt(0)
	v_mfma_f32_16x16x32_f16 v[4:7], v[32:35], v[36:39], v[4:7]
	v_mfma_f32_16x16x32_f16 v[28:31], v[32:35], v[44:47], v[28:31]
	ds_read_b128 v[32:35], v76
	v_mfma_f32_16x16x32_f16 v[24:27], v[40:43], v[36:39], v[24:27]
	v_mfma_f32_16x16x32_f16 v[20:23], v[40:43], v[44:47], v[20:23]
	ds_read_b128 v[36:39], v78
	ds_read_b128 v[40:43], v77
	ds_read_b128 v[44:47], v79
	s_waitcnt vmcnt(0)
	s_waitcnt lgkmcnt(0)
	s_barrier
	s_waitcnt lgkmcnt(0)
	v_mfma_f32_16x16x32_f16 v[4:7], v[32:35], v[36:39], v[4:7]
	v_mfma_f32_16x16x32_f16 v[28:31], v[32:35], v[44:47], v[28:31]
	ds_read_b128 v[32:35], v15
	v_mfma_f32_16x16x32_f16 v[24:27], v[40:43], v[36:39], v[24:27]
	v_mfma_f32_16x16x32_f16 v[20:23], v[40:43], v[44:47], v[20:23]
	ds_read_b128 v[36:39], v17 offset:8192
	ds_read_b128 v[40:43], v15 offset:2048
	ds_read_b128 v[44:47], v17 offset:10240
	s_waitcnt lgkmcnt(0)
	v_mfma_f32_16x16x32_f16 v[4:7], v[32:35], v[36:39], v[4:7]
	v_mfma_f32_16x16x32_f16 v[28:31], v[32:35], v[44:47], v[28:31]
	ds_read_b128 v[32:35], v16
	v_mfma_f32_16x16x32_f16 v[24:27], v[40:43], v[36:39], v[24:27]
	v_mfma_f32_16x16x32_f16 v[20:23], v[40:43], v[44:47], v[20:23]
	ds_read_b128 v[36:39], v18 offset:8192
	ds_read_b128 v[40:43], v16 offset:2048
	ds_read_b128 v[16:19], v18 offset:10240
	s_barrier
	s_waitcnt lgkmcnt(0)
	v_mfma_f32_16x16x32_f16 v[4:7], v[32:35], v[36:39], v[4:7]
	v_mfma_f32_16x16x32_f16 v[28:31], v[32:35], v[16:19], v[28:31]
	v_mfma_f32_16x16x32_f16 v[24:27], v[40:43], v[36:39], v[24:27]
	s_add_u32 s2, s10, s1
	s_addc_u32 s3, s11, 0
	v_mfma_f32_16x16x32_f16 v[14:17], v[40:43], v[16:19], v[20:23]
	s_nop 7
	v_pk_add_f32 v[4:5], v[124:125], v[4:5]
	v_pk_add_f32 v[6:7], v[126:127], v[6:7]
	ds_write_b128 v8, v[4:7]
	v_pk_add_f32 v[4:5], v[124:125], v[28:29]
	v_pk_add_f32 v[6:7], v[126:127], v[30:31]
	ds_write_b128 v8, v[4:7] offset:4096
	v_bitop3_b32 v4, v9, v12, 16 bitop3:0x36
	v_lshl_or_b32 v2, v4, 2, v2
	v_pk_add_f32 v[4:5], v[128:129], v[24:25]
	v_pk_add_f32 v[6:7], v[130:131], v[26:27]
	ds_write_b128 v2, v[4:7]
	v_pk_add_f32 v[4:5], v[128:129], v[14:15]
	v_pk_add_f32 v[6:7], v[130:131], v[16:17]
	ds_write_b128 v2, v[4:7] offset:4096
	v_or_b32_e32 v6, s0, v1
	v_and_b32_e32 v2, 0xf0, v11
	v_ashrrev_i32_e32 v7, 31, v6
	v_lshl_add_u64 v[12:13], s[2:3], 0, v[2:3]
	v_lshlrev_b32_e32 v2, 4, v10
	v_lshlrev_b64 v[6:7], 12, v[6:7]
	v_and_b32_e32 v14, 0xf0, v2
	v_lshl_add_u64 v[10:11], v[12:13], 0, v[6:7]
	v_or_b32_e32 v6, 0x200, v0
	v_lshl_or_b32 v2, v1, 8, v14
	v_lshrrev_b32_e32 v15, 4, v6
	s_waitcnt lgkmcnt(0)
	s_barrier
	ds_read_b128 v[2:5], v2
	v_xor_b32_e32 v6, v15, v0
	v_lshlrev_b32_e32 v6, 4, v6
	v_and_b32_e32 v6, 0xf0, v6
	v_lshl_or_b32 v6, v15, 8, v6
	ds_read_b128 v[6:9], v6
	s_waitcnt lgkmcnt(1)
	global_store_dwordx4 v[10:11], v[2:5], off nt
	v_or_b32_e32 v1, 64, v1
	s_nop 0
	v_or_b32_e32 v2, s0, v15
	v_ashrrev_i32_e32 v3, 31, v2
	v_lshlrev_b64 v[2:3], 12, v[2:3]
	v_lshl_add_u64 v[2:3], v[12:13], 0, v[2:3]
	s_waitcnt lgkmcnt(0)
	global_store_dwordx4 v[2:3], v[6:9], off nt
	v_lshl_or_b32 v2, v1, 8, v14
	ds_read_b128 v[2:5], v2
	v_or_b32_e32 v6, s0, v1
	v_or_b32_e32 v1, 0x600, v0
	v_lshrrev_b32_e32 v1, 4, v1
	v_xor_b32_e32 v0, v1, v0
	v_lshlrev_b32_e32 v0, 4, v0
	v_ashrrev_i32_e32 v7, 31, v6
	v_and_b32_e32 v0, 0xf0, v0
	v_lshlrev_b64 v[6:7], 12, v[6:7]
	v_lshl_or_b32 v0, v1, 8, v0
	v_lshl_add_u64 v[10:11], v[12:13], 0, v[6:7]
	ds_read_b128 v[6:9], v0
	v_or_b32_e32 v0, s0, v1
	v_ashrrev_i32_e32 v1, 31, v0
	v_lshlrev_b64 v[0:1], 12, v[0:1]
	v_lshl_add_u64 v[0:1], v[12:13], 0, v[0:1]
	s_waitcnt lgkmcnt(1)
	global_store_dwordx4 v[10:11], v[2:5], off nt
	s_waitcnt lgkmcnt(0)
	global_store_dwordx4 v[0:1], v[6:9], off nt
	s_endpgm

	.amdhsa_kernel _Z14outproj_kernelPKDF16_S0_PKfPf
		.amdhsa_group_segment_fixed_size 122880
		.amdhsa_private_segment_fixed_size 0
		.amdhsa_kernarg_size 32
		.amdhsa_user_sgpr_count 2
		.amdhsa_user_sgpr_dispatch_ptr 0
		.amdhsa_user_sgpr_queue_ptr 0
		.amdhsa_user_sgpr_kernarg_segment_ptr 1
		.amdhsa_user_sgpr_dispatch_id 0
		.amdhsa_user_sgpr_kernarg_preload_length 0
		.amdhsa_user_sgpr_kernarg_preload_offset 0
		.amdhsa_user_sgpr_private_segment_size 0
		.amdhsa_uses_dynamic_stack 0
		.amdhsa_enable_private_segment 0
		.amdhsa_system_sgpr_workgroup_id_x 1
		.amdhsa_system_sgpr_workgroup_id_y 0
		.amdhsa_system_sgpr_workgroup_id_z 0
		.amdhsa_system_sgpr_workgroup_info 0
		.amdhsa_system_vgpr_workitem_id 0
		.amdhsa_next_free_vgpr 169
		.amdhsa_next_free_sgpr 96
		.amdhsa_accum_offset 132
		.amdhsa_reserve_vcc 0
		.amdhsa_float_round_mode_32 0
		.amdhsa_float_round_mode_16_64 0
		.amdhsa_float_denorm_mode_32 3
		.amdhsa_float_denorm_mode_16_64 3
		.amdhsa_dx10_clamp 1
		.amdhsa_ieee_mode 1
		.amdhsa_fp16_overflow 0
		.amdhsa_tg_split 0
		.amdhsa_exception_fp_ieee_invalid_op 0
		.amdhsa_exception_fp_denorm_src 0
		.amdhsa_exception_fp_ieee_div_zero 0
		.amdhsa_exception_fp_ieee_overflow 0
		.amdhsa_exception_fp_ieee_underflow 0
		.amdhsa_exception_fp_ieee_inexact 0
		.amdhsa_exception_int_div_zero 0
	.end_amdhsa_kernel

amdhsa.kernels:
  - .agpr_count:     0
    .args:
      - .actual_access:  read_only
        .address_space:  global
        .offset:         0
        .size:           8
        .value_kind:     global_buffer
      - .actual_access:  read_only
        .address_space:  global
        .offset:         8
        .size:           8
        .value_kind:     global_buffer
      - .actual_access:  read_only
        .address_space:  global
        .offset:         16
        .size:           8
        .value_kind:     global_buffer
      - .actual_access:  read_only
        .address_space:  global
        .offset:         24
        .size:           8
        .value_kind:     global_buffer
      - .actual_access:  read_only
        .address_space:  global
        .offset:         32
        .size:           8
        .value_kind:     global_buffer
      - .actual_access:  read_only
        .address_space:  global
        .offset:         40
        .size:           8
        .value_kind:     global_buffer
      - .actual_access:  read_only
        .address_space:  global
        .offset:         48
        .size:           8
        .value_kind:     global_buffer
      - .address_space:  global
        .offset:         56
        .size:           8
        .value_kind:     global_buffer
      - .address_space:  global
        .offset:         64
        .size:           8
        .value_kind:     global_buffer
      - .actual_access:  read_only
        .address_space:  global
        .offset:         72
        .size:           8
        .value_kind:     global_buffer
      - .address_space:  global
        .offset:         80
        .size:           8
        .value_kind:     global_buffer
    .group_segment_fixed_size: 0
    .kernarg_segment_align: 8
    .kernarg_segment_size: 88
    .language:       OpenCL C
    .language_version:
      - 2
      - 0
    .max_flat_workgroup_size: 256
    .name:           _Z11prep_kernelPKfS0_S0_S0_S0_S0_S0_PDF16_S1_S1_S1_
    .private_segment_fixed_size: 0
    .sgpr_count:     23
    .sgpr_spill_count: 0
    .symbol:         _Z11prep_kernelPKfS0_S0_S0_S0_S0_S0_PDF16_S1_S1_S1_.kd
    .uniform_work_group_size: 1
    .uses_dynamic_stack: false
    .vgpr_count:     28
    .vgpr_spill_count: 0
    .wavefront_size: 64
  - .agpr_count:     0
    .args:
      - .offset:         0
        .size:           88
        .value_kind:     by_value
    .group_segment_fixed_size: 163840
    .kernarg_segment_align: 8
    .kernarg_segment_size: 88
    .language:       OpenCL C
    .language_version:
      - 2
      - 0
    .max_flat_workgroup_size: 512
    .name:           _Z12gemm1_kernel6G1Args
    .private_segment_fixed_size: 0
    .sgpr_count:     52
    .sgpr_spill_count: 0
    .symbol:         _Z12gemm1_kernel6G1Args.kd
    .uniform_work_group_size: 1
    .uses_dynamic_stack: false
    .vgpr_count:     144
    .vgpr_spill_count: 0
    .wavefront_size: 64
  - .agpr_count:     0
    .args:
      - .address_space:  global
        .offset:         0
        .size:           8
        .value_kind:     global_buffer
      - .address_space:  global
        .offset:         8
        .size:           8
        .value_kind:     global_buffer
      - .address_space:  global
        .offset:         16
        .size:           8
        .value_kind:     global_buffer
      - .actual_access:  read_only
        .address_space:  global
        .offset:         24
        .size:           8
        .value_kind:     global_buffer
      - .actual_access:  read_only
        .address_space:  global
        .offset:         32
        .size:           8
        .value_kind:     global_buffer
      - .actual_access:  read_only
        .address_space:  global
        .offset:         40
        .size:           8
        .value_kind:     global_buffer
      - .address_space:  global
        .offset:         48
        .size:           8
        .value_kind:     global_buffer
      - .actual_access:  read_only
        .address_space:  global
        .offset:         56
        .size:           8
        .value_kind:     global_buffer
      - .address_space:  global
        .offset:         64
        .size:           8
        .value_kind:     global_buffer
      - .actual_access:  read_only
        .address_space:  global
        .offset:         72
        .size:           8
        .value_kind:     global_buffer
      - .address_space:  global
        .offset:         80
        .size:           8
        .value_kind:     global_buffer
    .group_segment_fixed_size: 81920
    .kernarg_segment_align: 8
    .kernarg_segment_size: 88
    .language:       OpenCL C
    .language_version:
      - 2
      - 0
    .max_flat_workgroup_size: 512
    .name:           _Z11attn_kernelPKDF16_S0_S0_PKfS2_S2_S0_S2_PDF16_S2_S3_
    .private_segment_fixed_size: 0
    .sgpr_count:     62
    .sgpr_spill_count: 0
    .symbol:         _Z11attn_kernelPKDF16_S0_S0_PKfS2_S2_S0_S2_PDF16_S2_S3_.kd
    .uniform_work_group_size: 1
    .uses_dynamic_stack: false
    .vgpr_count:     126
    .vgpr_spill_count: 0
    .wavefront_size: 64
  - .agpr_count:     0
    .args:
      - .address_space:  global
        .offset:         0
        .size:           8
        .value_kind:     global_buffer
      - .address_space:  global
        .offset:         8
        .size:           8
        .value_kind:     global_buffer
      - .actual_access:  read_only
        .address_space:  global
        .offset:         16
        .size:           8
        .value_kind:     global_buffer
      - .actual_access:  write_only
        .address_space:  global
        .offset:         24
        .size:           8
        .value_kind:     global_buffer
    .group_segment_fixed_size: 122880
    .kernarg_segment_align: 8
    .kernarg_segment_size: 32
    .language:       OpenCL C
    .language_version:
      - 2
      - 0
    .max_flat_workgroup_size: 512
    .name:           _Z14outproj_kernelPKDF16_S0_PKfPf
    .private_segment_fixed_size: 0
    .sgpr_count:     31
    .sgpr_spill_count: 0
    .symbol:         _Z14outproj_kernelPKDF16_S0_PKfPf.kd
    .uniform_work_group_size: 1
    .uses_dynamic_stack: false
    .vgpr_count:     132
    .vgpr_spill_count: 0
    .wavefront_size: 64
